# LDS-DMA pieces moved from the QK/PV gap into the P.V section, one piece behind the third MFMA of each 32-column group (the read-free gaps left by the operand double-buffering)
# speedup vs baseline: 1.0098x; 1.0055x over previous
.LBB0_787:
	ds_read_b128 v[80:83], v134 offset:33792
	ds_read_b128 v[84:87], v134 offset:41984
	ds_read_b128 v[196:199], v135 offset:33792
	ds_read_b128 v[200:203], v135 offset:41984
	s_waitcnt lgkmcnt(2)
	v_mfma_f32_32x32x16_bf16 v[96:111], v[80:83], v[122:125], 0
	v_exp_f32_e32 v204, v72
	v_exp_f32_e32 v205, v73
	v_exp_f32_e32 v206, v74
	v_exp_f32_e32 v207, v75
	v_exp_f32_e32 v208, v76
	v_exp_f32_e32 v209, v77
	v_mfma_f32_32x32x16_bf16 v[80:95], v[84:87], v[122:125], 0
	v_exp_f32_e32 v210, v78
	v_exp_f32_e32 v79, v79
	s_waitcnt lgkmcnt(0)
	v_mfma_f32_32x32x16_bf16 v[96:111], v[196:199], v[126:129], v[96:111]
	v_mfma_f32_32x32x16_bf16 v[80:95], v[200:203], v[126:129], v[80:95]
	ds_read_b128 v[196:199], v136 offset:33792
	ds_read_b128 v[200:203], v136 offset:41984
	s_waitcnt lgkmcnt(0)
	v_mfma_f32_32x32x16_bf16 v[96:111], v[196:199], v[118:121], v[96:111]
	v_mfma_f32_32x32x16_bf16 v[80:95], v[200:203], v[118:121], v[80:95]
	ds_read_b128 v[196:199], v137 offset:33792
	ds_read_b128 v[200:203], v137 offset:41984
	v_exp_f32_e32 v180, v64
	v_add_f32_e32 v64, v161, v159
	v_add_f32_e32 v195, v157, v160
	v_add_f32_e32 v64, v155, v64
	v_add_f32_e32 v195, v158, v195
	v_add_f32_e32 v64, v154, v64
	v_add_f32_e32 v195, v156, v195
	v_add_f32_e32 v64, v151, v64
	v_add_f32_e32 v195, v153, v195
	v_add_f32_e32 v64, v149, v64
	v_add_f32_e32 v195, v152, v195
	v_add_f32_e32 v64, v147, v64
	s_waitcnt lgkmcnt(0)
	v_mfma_f32_32x32x16_bf16 v[96:111], v[196:199], v[114:117], v[96:111]
	v_exp_f32_e32 v197, v65
	v_add_f32_e32 v195, v150, v195
	v_exp_f32_e32 v198, v66
	v_add_f32_e32 v64, v146, v64
	v_exp_f32_e32 v199, v67
	v_add_f32_e32 v195, v148, v195
	v_add_f32_e32 v64, v180, v64
	v_mfma_f32_32x32x16_bf16 v[80:95], v[200:203], v[114:117], v[80:95]
	v_exp_f32_e32 v200, v68
	v_exp_f32_e32 v201, v69
	v_add_f32_e32 v195, v197, v195
	v_exp_f32_e32 v202, v70
	v_add_f32_e32 v64, v198, v64
	v_exp_f32_e32 v203, v71
	v_add_f32_e32 v195, v199, v195
	v_add_f32_e32 v64, v200, v64
	v_add_f32_e32 v195, v201, v195
	v_add_f32_e32 v64, v202, v64
	v_add_f32_e32 v195, v203, v195
	v_add_f32_e32 v64, v204, v64
	v_add_f32_e32 v195, v205, v195
	v_add_f32_e32 v64, v206, v64
	v_add_f32_e32 v195, v207, v195
	v_add_f32_e32 v64, v208, v64
	v_add_f32_e32 v195, v209, v195
	v_add_f32_e32 v64, v210, v64
	v_add_f32_e32 v195, v79, v195
	v_add_f32_e32 v195, v195, v64
	v_cvt_pk_bf16_f32 v64, v159, v161
	v_cvt_pk_bf16_f32 v65, v157, v160
	v_cvt_pk_bf16_f32 v66, v155, v158
	v_cvt_pk_bf16_f32 v67, v154, v156
	v_cvt_pk_bf16_f32 v68, v151, v153
	v_cvt_pk_bf16_f32 v69, v149, v152
	v_cvt_pk_bf16_f32 v70, v147, v150
	v_cvt_pk_bf16_f32 v71, v146, v148
	v_cvt_pk_bf16_f32 v72, v180, v197
	v_cvt_pk_bf16_f32 v73, v198, v199
	v_cvt_pk_bf16_f32 v74, v200, v201
	v_cvt_pk_bf16_f32 v75, v202, v203
	v_cvt_pk_bf16_f32 v76, v204, v205
	v_cvt_pk_bf16_f32 v77, v206, v207
	v_cvt_pk_bf16_f32 v78, v208, v209
	v_cvt_pk_bf16_f32 v79, v210, v79
	ds_read_b64_tr_b16 v[198:199], v192 offset:1024
	ds_read_b64_tr_b16 v[200:201], v192 offset:3072
	ds_read_b64_tr_b16 v[202:203], v192 offset:5120
	ds_read_b64_tr_b16 v[204:205], v192 offset:7168
	ds_read_b64_tr_b16 v[206:207], v192 offset:9216
	ds_read_b64_tr_b16 v[208:209], v192 offset:11264
	ds_read_b64_tr_b16 v[222:223], v192 offset:13312
	ds_read_b64_tr_b16 v[224:225], v192 offset:15360
	s_waitcnt lgkmcnt(0)
	v_mfma_f32_32x32x16_bf16 v[0:15], v[64:67], v[198:201], v[0:15]
	ds_read_b64_tr_b16 v[198:199], v192 offset:1536
	ds_read_b64_tr_b16 v[200:201], v192 offset:3584
	ds_read_b64_tr_b16 v[138:139], v192 offset:9728
	ds_read_b64_tr_b16 v[140:141], v192 offset:11776
	v_mfma_f32_32x32x16_bf16 v[0:15], v[68:71], v[202:205], v[0:15]
	ds_read_b64_tr_b16 v[202:203], v192 offset:5632
	ds_read_b64_tr_b16 v[204:205], v192 offset:7680
	ds_read_b64_tr_b16 v[142:143], v192 offset:13824
	ds_read_b64_tr_b16 v[144:145], v192 offset:15872
	v_mfma_f32_32x32x16_bf16 v[0:15], v[72:75], v[206:209], v[0:15]
	s_add_i32 m0, s84, 0x8400
	s_add_u32 s66, s78, s65
	s_addc_u32 s67, s79, 0
	global_load_lds_dwordx4 v185, s[66:67]
	v_mfma_f32_32x32x16_bf16 v[0:15], v[76:79], v[222:225], v[0:15]
	s_waitcnt lgkmcnt(0)
	v_mfma_f32_32x32x16_bf16 v[48:63], v[64:67], v[198:201], v[48:63]
	ds_read_b64_tr_b16 v[198:199], v192 offset:2048
	ds_read_b64_tr_b16 v[200:201], v192 offset:4096
	ds_read_b64_tr_b16 v[206:207], v192 offset:10240
	ds_read_b64_tr_b16 v[208:209], v192 offset:12288
	v_mfma_f32_32x32x16_bf16 v[48:63], v[68:71], v[202:205], v[48:63]
	ds_read_b64_tr_b16 v[202:203], v192 offset:6144
	ds_read_b64_tr_b16 v[204:205], v192 offset:8192
	ds_read_b64_tr_b16 v[222:223], v192 offset:14336
	ds_read_b64_tr_b16 v[224:225], v192 offset:16384
	v_mfma_f32_32x32x16_bf16 v[48:63], v[72:75], v[138:141], v[48:63]
	s_add_i32 m0, s84, 0xa400
	s_add_i32 s64, s65, 0x60000
	global_load_lds_dwordx4 v184, s[66:67]
	v_mfma_f32_32x32x16_bf16 v[48:63], v[76:79], v[142:145], v[48:63]
	s_waitcnt lgkmcnt(0)
	v_mfma_f32_32x32x16_bf16 v[32:47], v[64:67], v[198:201], v[32:47]
	ds_read_b64_tr_b16 v[198:199], v192 offset:2560
	ds_read_b64_tr_b16 v[200:201], v192 offset:4608
	ds_read_b64_tr_b16 v[138:139], v192 offset:10752
	ds_read_b64_tr_b16 v[140:141], v192 offset:12800
	v_mfma_f32_32x32x16_bf16 v[32:47], v[68:71], v[202:205], v[32:47]
	ds_read_b64_tr_b16 v[202:203], v192 offset:6656
	ds_read_b64_tr_b16 v[204:205], v192 offset:8704
	ds_read_b64_tr_b16 v[142:143], v192 offset:14848
	ds_read_b64_tr_b16 v[144:145], v192 offset:16896
	v_mfma_f32_32x32x16_bf16 v[32:47], v[72:75], v[206:209], v[32:47]
	s_add_i32 m0, s84, 0xc400
	s_add_u32 s70, s80, s64
	s_addc_u32 s71, s81, 0
	global_load_lds_dwordx4 v183, s[70:71]
	v_mfma_f32_32x32x16_bf16 v[32:47], v[76:79], v[222:225], v[32:47]
	s_waitcnt lgkmcnt(0)
	v_mfma_f32_32x32x16_bf16 v[16:31], v[64:67], v[198:201], v[16:31]
	v_max_f32_e32 v64, v96, v97
	v_max3_f32 v65, v80, v81, v82
	v_max3_f32 v64, v64, v98, v99
	v_max3_f32 v65, v65, v83, v84
	v_max3_f32 v64, v64, v100, v101
	v_mfma_f32_32x32x16_bf16 v[16:31], v[68:71], v[202:205], v[16:31]
	v_max3_f32 v65, v65, v85, v86
	v_max3_f32 v64, v64, v102, v103
	v_max3_f32 v65, v65, v87, v88
	v_max3_f32 v64, v64, v104, v105
	v_max3_f32 v65, v65, v89, v90
	v_max3_f32 v64, v64, v106, v107
	v_max3_f32 v65, v65, v91, v92
	v_mfma_f32_32x32x16_bf16 v[16:31], v[72:75], v[138:141], v[16:31]
	s_add_i32 m0, s84, 0xe400
	s_mov_b32 s65, s64
	global_load_lds_dwordx4 v182, s[70:71]
	v_max3_f32 v64, v64, v108, v109
	v_max3_f32 v65, v65, v93, v94
	v_max3_f32 v64, v64, v110, v111
	v_max3_f32 v64, v64, v65, v95
	v_mov_b32_e32 v198, 1.0
	v_mfma_f32_32x32x16_bf16 v[16:31], v[76:79], v[142:145], v[16:31]
	v_cmp_ge_f32_e64 s[0:1], s56, v64
	s_cmp_eq_u64 s[0:1], exec
	s_cbranch_scc1 .LBB0_792
	s_branch .LBB0_801

.LBB0_792:
	v_exp_f32_e32 v197, v96
	v_exp_f32_e32 v208, v97
	v_exp_f32_e32 v209, v98
	v_exp_f32_e32 v210, v99
	v_exp_f32_e32 v211, v100
	v_exp_f32_e32 v220, v101
	v_exp_f32_e32 v221, v102
	v_exp_f32_e32 v222, v103
	v_exp_f32_e32 v223, v104
	v_exp_f32_e32 v224, v105
	v_exp_f32_e32 v225, v106
	v_exp_f32_e32 v226, v107
	v_exp_f32_e32 v227, v108
	v_exp_f32_e32 v228, v109
	v_exp_f32_e32 v229, v110
	v_exp_f32_e32 v230, v111
	s_waitcnt vmcnt(4) lgkmcnt(0)
	s_barrier
	ds_read_b128 v[64:67], v134 offset:50176
	ds_read_b128 v[68:71], v134 offset:58368
	ds_read_b128 v[200:203], v135 offset:50176
	ds_read_b128 v[204:207], v135 offset:58368
	v_exp_f32_e32 v231, v87
	s_waitcnt lgkmcnt(2)
	v_mfma_f32_32x32x16_bf16 v[96:111], v[64:67], v[122:125], 0
	v_exp_f32_e32 v232, v88
	v_exp_f32_e32 v233, v89
	v_exp_f32_e32 v234, v90
	v_exp_f32_e32 v235, v91
	v_exp_f32_e32 v236, v92
	v_exp_f32_e32 v237, v93
	v_exp_f32_e32 v238, v94
	v_mfma_f32_32x32x16_bf16 v[64:79], v[68:71], v[122:125], 0
	v_exp_f32_e32 v95, v95
	s_waitcnt lgkmcnt(0)
	v_mfma_f32_32x32x16_bf16 v[96:111], v[200:203], v[126:129], v[96:111]
	v_mfma_f32_32x32x16_bf16 v[64:79], v[204:207], v[126:129], v[64:79]
	ds_read_b128 v[200:203], v136 offset:50176
	ds_read_b128 v[204:207], v136 offset:58368
	s_waitcnt lgkmcnt(0)
	v_mfma_f32_32x32x16_bf16 v[96:111], v[200:203], v[118:121], v[96:111]
	v_mfma_f32_32x32x16_bf16 v[64:79], v[204:207], v[118:121], v[64:79]
	ds_read_b128 v[200:203], v137 offset:50176
	ds_read_b128 v[204:207], v137 offset:58368
	s_waitcnt lgkmcnt(0)
	v_mfma_f32_32x32x16_bf16 v[96:111], v[200:203], v[114:117], v[96:111]
	v_exp_f32_e32 v201, v80
	v_add_f32_e32 v80, v208, v197
	v_add_f32_e32 v199, v209, v210
	v_add_f32_e32 v80, v211, v80
	v_add_f32_e32 v199, v220, v199
	v_add_f32_e32 v80, v221, v80
	v_add_f32_e32 v199, v222, v199
	v_add_f32_e32 v80, v223, v80
	v_add_f32_e32 v199, v224, v199
	v_add_f32_e32 v80, v225, v80
	v_add_f32_e32 v199, v226, v199
	v_add_f32_e32 v80, v227, v80
	v_exp_f32_e32 v202, v81
	v_add_f32_e32 v199, v228, v199
	v_exp_f32_e32 v203, v82
	v_add_f32_e32 v80, v229, v80
	v_mfma_f32_32x32x16_bf16 v[64:79], v[204:207], v[114:117], v[64:79]
	v_exp_f32_e32 v204, v83
	v_add_f32_e32 v199, v230, v199
	v_exp_f32_e32 v205, v84
	v_add_f32_e32 v80, v201, v80
	v_exp_f32_e32 v206, v85
	v_add_f32_e32 v199, v202, v199
	v_exp_f32_e32 v207, v86
	v_add_f32_e32 v80, v203, v80
	v_add_f32_e32 v199, v204, v199
	v_add_f32_e32 v80, v205, v80
	v_add_f32_e32 v199, v206, v199
	v_add_f32_e32 v80, v207, v80
	v_add_f32_e32 v199, v231, v199
	v_add_f32_e32 v80, v232, v80
	v_add_f32_e32 v199, v233, v199
	v_add_f32_e32 v80, v234, v80
	v_add_f32_e32 v199, v235, v199
	v_add_f32_e32 v80, v236, v80
	v_add_f32_e32 v199, v237, v199
	v_add_f32_e32 v80, v238, v80
	v_add_f32_e32 v199, v95, v199
	v_add_f32_e32 v199, v199, v80
	v_cvt_pk_bf16_f32 v80, v197, v208
	v_cvt_pk_bf16_f32 v81, v209, v210
	v_cvt_pk_bf16_f32 v82, v211, v220
	v_cvt_pk_bf16_f32 v83, v221, v222
	v_cvt_pk_bf16_f32 v84, v223, v224
	v_cvt_pk_bf16_f32 v85, v225, v226
	v_cvt_pk_bf16_f32 v86, v227, v228
	v_cvt_pk_bf16_f32 v87, v229, v230
	v_cvt_pk_bf16_f32 v88, v201, v202
	v_cvt_pk_bf16_f32 v89, v203, v204
	v_cvt_pk_bf16_f32 v90, v205, v206
	v_cvt_pk_bf16_f32 v91, v207, v231
	v_cvt_pk_bf16_f32 v92, v232, v233
	v_cvt_pk_bf16_f32 v93, v234, v235
	v_cvt_pk_bf16_f32 v94, v236, v237
	v_cvt_pk_bf16_f32 v95, v238, v95
.LBB0_794:
	ds_read_b64_tr_b16 v[202:203], v192 offset:17408
	ds_read_b64_tr_b16 v[204:205], v192 offset:19456
	ds_read_b64_tr_b16 v[206:207], v192 offset:21504
	ds_read_b64_tr_b16 v[208:209], v192 offset:23552
	ds_read_b64_tr_b16 v[222:223], v192 offset:25600
	ds_read_b64_tr_b16 v[224:225], v192 offset:27648
	ds_read_b64_tr_b16 v[226:227], v192 offset:29696
	ds_read_b64_tr_b16 v[228:229], v192 offset:31744
	s_waitcnt lgkmcnt(0)
	v_mfma_f32_32x32x16_bf16 v[0:15], v[80:83], v[202:205], v[0:15]
	ds_read_b64_tr_b16 v[202:203], v192 offset:17920
	ds_read_b64_tr_b16 v[204:205], v192 offset:19968
	ds_read_b64_tr_b16 v[138:139], v192 offset:26112
	ds_read_b64_tr_b16 v[140:141], v192 offset:28160
	v_mfma_f32_32x32x16_bf16 v[0:15], v[84:87], v[206:209], v[0:15]
	ds_read_b64_tr_b16 v[206:207], v192 offset:22016
	ds_read_b64_tr_b16 v[208:209], v192 offset:24064
	ds_read_b64_tr_b16 v[142:143], v192 offset:30208
	ds_read_b64_tr_b16 v[144:145], v192 offset:32256
	v_mfma_f32_32x32x16_bf16 v[0:15], v[88:91], v[222:225], v[0:15]
	s_add_i32 m0, s84, 0x400
	s_add_u32 s66, s78, s65
	s_addc_u32 s67, s79, 0
	global_load_lds_dwordx4 v185, s[66:67]
	v_mfma_f32_32x32x16_bf16 v[0:15], v[92:95], v[226:229], v[0:15]
	s_waitcnt lgkmcnt(0)
	v_mfma_f32_32x32x16_bf16 v[48:63], v[80:83], v[202:205], v[48:63]
	ds_read_b64_tr_b16 v[202:203], v192 offset:18432
	ds_read_b64_tr_b16 v[204:205], v192 offset:20480
	ds_read_b64_tr_b16 v[222:223], v192 offset:26624
	ds_read_b64_tr_b16 v[224:225], v192 offset:28672
	v_mfma_f32_32x32x16_bf16 v[48:63], v[84:87], v[206:209], v[48:63]
	ds_read_b64_tr_b16 v[206:207], v192 offset:22528
	ds_read_b64_tr_b16 v[208:209], v192 offset:24576
	ds_read_b64_tr_b16 v[226:227], v192 offset:30720
	ds_read_b64_tr_b16 v[228:229], v192 offset:32768
	v_mfma_f32_32x32x16_bf16 v[48:63], v[88:91], v[138:141], v[48:63]
	s_add_i32 m0, s84, 0x2400
	s_add_i32 s64, s65, 0x60000
	global_load_lds_dwordx4 v184, s[66:67]
	v_mfma_f32_32x32x16_bf16 v[48:63], v[92:95], v[142:145], v[48:63]
	s_waitcnt lgkmcnt(0)
	v_mfma_f32_32x32x16_bf16 v[32:47], v[80:83], v[202:205], v[32:47]
	ds_read_b64_tr_b16 v[202:203], v192 offset:18944
	ds_read_b64_tr_b16 v[204:205], v192 offset:20992
	ds_read_b64_tr_b16 v[138:139], v192 offset:27136
	ds_read_b64_tr_b16 v[140:141], v192 offset:29184
	v_mfma_f32_32x32x16_bf16 v[32:47], v[84:87], v[206:209], v[32:47]
	ds_read_b64_tr_b16 v[206:207], v192 offset:23040
	ds_read_b64_tr_b16 v[208:209], v192 offset:25088
	ds_read_b64_tr_b16 v[142:143], v192 offset:31232
	ds_read_b64_tr_b16 v[144:145], v192 offset:33280
	v_mfma_f32_32x32x16_bf16 v[32:47], v[88:91], v[222:225], v[32:47]
	s_cmp_eq_u32 s55, 29
	s_cselect_b32 s64, s89, s64
	s_add_i32 m0, s84, 0x10400
	s_add_u32 s70, s80, s64
	s_addc_u32 s71, s81, 0
	global_load_lds_dwordx4 v183, s[70:71]
	v_mfma_f32_32x32x16_bf16 v[32:47], v[92:95], v[226:229], v[32:47]
	s_waitcnt lgkmcnt(0)
	v_mfma_f32_32x32x16_bf16 v[16:31], v[80:83], v[202:205], v[16:31]
	v_max_f32_e32 v80, v96, v97
	v_max3_f32 v81, v64, v65, v66
	v_max3_f32 v80, v80, v98, v99
	v_max3_f32 v81, v81, v67, v68
	v_max3_f32 v80, v80, v100, v101
	v_mfma_f32_32x32x16_bf16 v[16:31], v[84:87], v[206:209], v[16:31]
	v_max3_f32 v81, v81, v69, v70
	v_max3_f32 v80, v80, v102, v103
	v_max3_f32 v81, v81, v71, v72
	v_max3_f32 v80, v80, v104, v105
	v_max3_f32 v81, v81, v73, v74
	v_max3_f32 v80, v80, v106, v107
	v_max3_f32 v81, v81, v75, v76
	v_mfma_f32_32x32x16_bf16 v[16:31], v[88:91], v[138:141], v[16:31]
	s_add_i32 m0, s84, 0x12400
	s_mov_b32 s65, s64
	global_load_lds_dwordx4 v182, s[70:71]
	v_max3_f32 v80, v80, v108, v109
	v_max3_f32 v81, v81, v77, v78
	v_max3_f32 v80, v80, v110, v111
	v_max3_f32 v80, v80, v81, v79
	v_mov_b32_e32 v197, 1.0
	v_mfma_f32_32x32x16_bf16 v[16:31], v[92:95], v[142:145], v[16:31]
	v_cmp_ge_f32_e64 s[0:1], s56, v80
	s_cmp_eq_u64 s[0:1], exec
	s_cbranch_scc1 .LBB0_799
	s_branch .LBB0_802

.LBB0_799:
	v_exp_f32_e32 v159, v96
	v_exp_f32_e32 v161, v97
	v_exp_f32_e32 v157, v98
	v_exp_f32_e32 v160, v99
	v_exp_f32_e32 v155, v100
	v_exp_f32_e32 v158, v101
	v_exp_f32_e32 v154, v102
	v_exp_f32_e32 v156, v103
	v_exp_f32_e32 v151, v104
	v_exp_f32_e32 v153, v105
	v_exp_f32_e32 v149, v106
	v_exp_f32_e32 v152, v107
	v_exp_f32_e32 v147, v108
	v_exp_f32_e32 v150, v109
	v_exp_f32_e32 v146, v110
	v_exp_f32_e32 v148, v111
	v_fma_f32 v80, v193, v179, v195
	v_fma_f32 v179, v80, v198, v199
	s_cmp_gt_u32 s55, 32
	s_waitcnt vmcnt(4) lgkmcnt(0)
	s_barrier
	s_cbranch_scc1 .LBB0_803
	s_add_i32 s55, s55, 2
	v_mov_b32_e32 v193, v197
	ds_read_b128 v[80:83], v130 offset:50176
	ds_read_b128 v[84:87], v130 offset:58368
	ds_read_b128 v[196:199], v131 offset:50176
	ds_read_b128 v[200:203], v131 offset:58368
	s_waitcnt lgkmcnt(2)
	v_mfma_f32_32x32x16_bf16 v[96:111], v[80:83], v[122:125], 0
	v_exp_f32_e32 v204, v72
	v_exp_f32_e32 v205, v73
	v_exp_f32_e32 v206, v74
	v_exp_f32_e32 v207, v75
	v_exp_f32_e32 v208, v76
	v_exp_f32_e32 v209, v77
	v_mfma_f32_32x32x16_bf16 v[80:95], v[84:87], v[122:125], 0
	v_exp_f32_e32 v210, v78
	v_exp_f32_e32 v79, v79
	s_waitcnt lgkmcnt(0)
	v_mfma_f32_32x32x16_bf16 v[96:111], v[196:199], v[126:129], v[96:111]
	v_mfma_f32_32x32x16_bf16 v[80:95], v[200:203], v[126:129], v[80:95]
	ds_read_b128 v[196:199], v132 offset:50176
	ds_read_b128 v[200:203], v132 offset:58368
	s_waitcnt lgkmcnt(0)
	v_mfma_f32_32x32x16_bf16 v[96:111], v[196:199], v[118:121], v[96:111]
	v_mfma_f32_32x32x16_bf16 v[80:95], v[200:203], v[118:121], v[80:95]
	ds_read_b128 v[196:199], v133 offset:50176
	ds_read_b128 v[200:203], v133 offset:58368
	v_exp_f32_e32 v180, v64
	v_add_f32_e32 v64, v161, v159
	v_add_f32_e32 v195, v157, v160
	v_add_f32_e32 v64, v155, v64
	v_add_f32_e32 v195, v158, v195
	v_add_f32_e32 v64, v154, v64
	v_add_f32_e32 v195, v156, v195
	v_add_f32_e32 v64, v151, v64
	v_add_f32_e32 v195, v153, v195
	v_add_f32_e32 v64, v149, v64
	v_add_f32_e32 v195, v152, v195
	v_add_f32_e32 v64, v147, v64
	s_waitcnt lgkmcnt(0)
	v_mfma_f32_32x32x16_bf16 v[96:111], v[196:199], v[114:117], v[96:111]
	v_exp_f32_e32 v197, v65
	v_add_f32_e32 v195, v150, v195
	v_exp_f32_e32 v198, v66
	v_add_f32_e32 v64, v146, v64
	v_exp_f32_e32 v199, v67
	v_add_f32_e32 v195, v148, v195
	v_add_f32_e32 v64, v180, v64
	v_mfma_f32_32x32x16_bf16 v[80:95], v[200:203], v[114:117], v[80:95]
	v_exp_f32_e32 v200, v68
	v_exp_f32_e32 v201, v69
	v_add_f32_e32 v195, v197, v195
	v_exp_f32_e32 v202, v70
	v_add_f32_e32 v64, v198, v64
	v_exp_f32_e32 v203, v71
	v_add_f32_e32 v195, v199, v195
	v_add_f32_e32 v64, v200, v64
	v_add_f32_e32 v195, v201, v195
	v_add_f32_e32 v64, v202, v64
	v_add_f32_e32 v195, v203, v195
	v_add_f32_e32 v64, v204, v64
	v_add_f32_e32 v195, v205, v195
	v_add_f32_e32 v64, v206, v64
	v_add_f32_e32 v195, v207, v195
	v_add_f32_e32 v64, v208, v64
	v_add_f32_e32 v195, v209, v195
	v_add_f32_e32 v64, v210, v64
	v_add_f32_e32 v195, v79, v195
	v_add_f32_e32 v195, v195, v64
	v_cvt_pk_bf16_f32 v64, v159, v161
	v_cvt_pk_bf16_f32 v65, v157, v160
	v_cvt_pk_bf16_f32 v66, v155, v158
	v_cvt_pk_bf16_f32 v67, v154, v156
	v_cvt_pk_bf16_f32 v68, v151, v153
	v_cvt_pk_bf16_f32 v69, v149, v152
	v_cvt_pk_bf16_f32 v70, v147, v150
	v_cvt_pk_bf16_f32 v71, v146, v148
	v_cvt_pk_bf16_f32 v72, v180, v197
	v_cvt_pk_bf16_f32 v73, v198, v199
	v_cvt_pk_bf16_f32 v74, v200, v201
	v_cvt_pk_bf16_f32 v75, v202, v203
	v_cvt_pk_bf16_f32 v76, v204, v205
	v_cvt_pk_bf16_f32 v77, v206, v207
	v_cvt_pk_bf16_f32 v78, v208, v209
	v_cvt_pk_bf16_f32 v79, v210, v79
	ds_read_b64_tr_b16 v[198:199], v192 offset:33792
	ds_read_b64_tr_b16 v[200:201], v192 offset:35840
	ds_read_b64_tr_b16 v[202:203], v192 offset:37888
	ds_read_b64_tr_b16 v[204:205], v192 offset:39936
	ds_read_b64_tr_b16 v[206:207], v192 offset:41984
	ds_read_b64_tr_b16 v[208:209], v192 offset:44032
	ds_read_b64_tr_b16 v[222:223], v192 offset:46080
	ds_read_b64_tr_b16 v[224:225], v192 offset:48128
	s_waitcnt lgkmcnt(0)
	v_mfma_f32_32x32x16_bf16 v[0:15], v[64:67], v[198:201], v[0:15]
	ds_read_b64_tr_b16 v[198:199], v192 offset:34304
	ds_read_b64_tr_b16 v[200:201], v192 offset:36352
	ds_read_b64_tr_b16 v[138:139], v192 offset:42496
	ds_read_b64_tr_b16 v[140:141], v192 offset:44544
	v_mfma_f32_32x32x16_bf16 v[0:15], v[68:71], v[202:205], v[0:15]
	ds_read_b64_tr_b16 v[202:203], v192 offset:38400
	ds_read_b64_tr_b16 v[204:205], v192 offset:40448
	ds_read_b64_tr_b16 v[142:143], v192 offset:46592
	ds_read_b64_tr_b16 v[144:145], v192 offset:48640
	v_mfma_f32_32x32x16_bf16 v[0:15], v[72:75], v[206:209], v[0:15]
	s_add_i32 m0, s84, 0x4400
	s_add_u32 s66, s78, s65
	s_addc_u32 s67, s79, 0
	global_load_lds_dwordx4 v185, s[66:67]
	v_mfma_f32_32x32x16_bf16 v[0:15], v[76:79], v[222:225], v[0:15]
	s_waitcnt lgkmcnt(0)
	v_mfma_f32_32x32x16_bf16 v[48:63], v[64:67], v[198:201], v[48:63]
	ds_read_b64_tr_b16 v[198:199], v192 offset:34816
	ds_read_b64_tr_b16 v[200:201], v192 offset:36864
	ds_read_b64_tr_b16 v[206:207], v192 offset:43008
	ds_read_b64_tr_b16 v[208:209], v192 offset:45056
	v_mfma_f32_32x32x16_bf16 v[48:63], v[68:71], v[202:205], v[48:63]
	ds_read_b64_tr_b16 v[202:203], v192 offset:38912
	ds_read_b64_tr_b16 v[204:205], v192 offset:40960
	ds_read_b64_tr_b16 v[222:223], v192 offset:47104
	ds_read_b64_tr_b16 v[224:225], v192 offset:49152
	v_mfma_f32_32x32x16_bf16 v[48:63], v[72:75], v[138:141], v[48:63]
	s_add_i32 m0, s84, 0x6400
	s_add_i32 s64, s65, 0x60000
	global_load_lds_dwordx4 v184, s[66:67]
	v_mfma_f32_32x32x16_bf16 v[48:63], v[76:79], v[142:145], v[48:63]
	s_waitcnt lgkmcnt(0)
	v_mfma_f32_32x32x16_bf16 v[32:47], v[64:67], v[198:201], v[32:47]
	ds_read_b64_tr_b16 v[198:199], v192 offset:35328
	ds_read_b64_tr_b16 v[200:201], v192 offset:37376
	ds_read_b64_tr_b16 v[138:139], v192 offset:43520
	ds_read_b64_tr_b16 v[140:141], v192 offset:45568
	v_mfma_f32_32x32x16_bf16 v[32:47], v[68:71], v[202:205], v[32:47]
	ds_read_b64_tr_b16 v[202:203], v192 offset:39424
	ds_read_b64_tr_b16 v[204:205], v192 offset:41472
	ds_read_b64_tr_b16 v[142:143], v192 offset:47616
	ds_read_b64_tr_b16 v[144:145], v192 offset:49664
	v_mfma_f32_32x32x16_bf16 v[32:47], v[72:75], v[206:209], v[32:47]
	s_add_i32 m0, s84, 0x14400
	s_add_u32 s70, s80, s64
	s_addc_u32 s71, s81, 0
	global_load_lds_dwordx4 v183, s[70:71]
	v_mfma_f32_32x32x16_bf16 v[32:47], v[76:79], v[222:225], v[32:47]
	s_waitcnt lgkmcnt(0)
	v_mfma_f32_32x32x16_bf16 v[16:31], v[64:67], v[198:201], v[16:31]
	v_max_f32_e32 v64, v96, v97
	v_max3_f32 v65, v80, v81, v82
	v_max3_f32 v64, v64, v98, v99
	v_max3_f32 v65, v65, v83, v84
	v_max3_f32 v64, v64, v100, v101
	v_mfma_f32_32x32x16_bf16 v[16:31], v[68:71], v[202:205], v[16:31]
	v_max3_f32 v65, v65, v85, v86
	v_max3_f32 v64, v64, v102, v103
	v_max3_f32 v65, v65, v87, v88
	v_max3_f32 v64, v64, v104, v105
	v_max3_f32 v65, v65, v89, v90
	v_max3_f32 v64, v64, v106, v107
	v_max3_f32 v65, v65, v91, v92
	v_mfma_f32_32x32x16_bf16 v[16:31], v[72:75], v[138:141], v[16:31]
	s_add_i32 m0, s84, 0x16400
	s_mov_b32 s65, s64
	global_load_lds_dwordx4 v182, s[70:71]
	v_max3_f32 v64, v64, v108, v109
	v_max3_f32 v65, v65, v93, v94
	v_max3_f32 v64, v64, v110, v111
	v_max3_f32 v64, v64, v65, v95
	v_mov_b32_e32 v198, 1.0
	v_mfma_f32_32x32x16_bf16 v[16:31], v[76:79], v[142:145], v[16:31]
	v_cmp_ge_f32_e64 s[0:1], s56, v64
	s_cmp_eq_u64 s[0:1], exec
	s_cbranch_scc1 .Lc1_792
	s_branch .Lc1_801

.Lc1_792:
	v_exp_f32_e32 v197, v96
	v_exp_f32_e32 v208, v97
	v_exp_f32_e32 v209, v98
	v_exp_f32_e32 v210, v99
	v_exp_f32_e32 v211, v100
	v_exp_f32_e32 v220, v101
	v_exp_f32_e32 v221, v102
	v_exp_f32_e32 v222, v103
	v_exp_f32_e32 v223, v104
	v_exp_f32_e32 v224, v105
	v_exp_f32_e32 v225, v106
	v_exp_f32_e32 v226, v107
	v_exp_f32_e32 v227, v108
	v_exp_f32_e32 v228, v109
	v_exp_f32_e32 v229, v110
	v_exp_f32_e32 v230, v111
	s_waitcnt vmcnt(4) lgkmcnt(0)
	s_barrier
	ds_read_b128 v[64:67], v134 offset:33792
	ds_read_b128 v[68:71], v134 offset:41984
	ds_read_b128 v[200:203], v135 offset:33792
	ds_read_b128 v[204:207], v135 offset:41984
	v_exp_f32_e32 v231, v87
	s_waitcnt lgkmcnt(2)
	v_mfma_f32_32x32x16_bf16 v[96:111], v[64:67], v[122:125], 0
	v_exp_f32_e32 v232, v88
	v_exp_f32_e32 v233, v89
	v_exp_f32_e32 v234, v90
	v_exp_f32_e32 v235, v91
	v_exp_f32_e32 v236, v92
	v_exp_f32_e32 v237, v93
	v_exp_f32_e32 v238, v94
	v_mfma_f32_32x32x16_bf16 v[64:79], v[68:71], v[122:125], 0
	v_exp_f32_e32 v95, v95
	s_waitcnt lgkmcnt(0)
	v_mfma_f32_32x32x16_bf16 v[96:111], v[200:203], v[126:129], v[96:111]
	v_mfma_f32_32x32x16_bf16 v[64:79], v[204:207], v[126:129], v[64:79]
	ds_read_b128 v[200:203], v136 offset:33792
	ds_read_b128 v[204:207], v136 offset:41984
	s_waitcnt lgkmcnt(0)
	v_mfma_f32_32x32x16_bf16 v[96:111], v[200:203], v[118:121], v[96:111]
	v_mfma_f32_32x32x16_bf16 v[64:79], v[204:207], v[118:121], v[64:79]
	ds_read_b128 v[200:203], v137 offset:33792
	ds_read_b128 v[204:207], v137 offset:41984
	s_waitcnt lgkmcnt(0)
	v_mfma_f32_32x32x16_bf16 v[96:111], v[200:203], v[114:117], v[96:111]
	v_exp_f32_e32 v201, v80
	v_add_f32_e32 v80, v208, v197
	v_add_f32_e32 v199, v209, v210
	v_add_f32_e32 v80, v211, v80
	v_add_f32_e32 v199, v220, v199
	v_add_f32_e32 v80, v221, v80
	v_add_f32_e32 v199, v222, v199
	v_add_f32_e32 v80, v223, v80
	v_add_f32_e32 v199, v224, v199
	v_add_f32_e32 v80, v225, v80
	v_add_f32_e32 v199, v226, v199
	v_add_f32_e32 v80, v227, v80
	v_exp_f32_e32 v202, v81
	v_add_f32_e32 v199, v228, v199
	v_exp_f32_e32 v203, v82
	v_add_f32_e32 v80, v229, v80
	v_mfma_f32_32x32x16_bf16 v[64:79], v[204:207], v[114:117], v[64:79]
	v_exp_f32_e32 v204, v83
	v_add_f32_e32 v199, v230, v199
	v_exp_f32_e32 v205, v84
	v_add_f32_e32 v80, v201, v80
	v_exp_f32_e32 v206, v85
	v_add_f32_e32 v199, v202, v199
	v_exp_f32_e32 v207, v86
	v_add_f32_e32 v80, v203, v80
	v_add_f32_e32 v199, v204, v199
	v_add_f32_e32 v80, v205, v80
	v_add_f32_e32 v199, v206, v199
	v_add_f32_e32 v80, v207, v80
	v_add_f32_e32 v199, v231, v199
	v_add_f32_e32 v80, v232, v80
	v_add_f32_e32 v199, v233, v199
	v_add_f32_e32 v80, v234, v80
	v_add_f32_e32 v199, v235, v199
	v_add_f32_e32 v80, v236, v80
	v_add_f32_e32 v199, v237, v199
	v_add_f32_e32 v80, v238, v80
	v_add_f32_e32 v199, v95, v199
	v_add_f32_e32 v199, v199, v80
	v_cvt_pk_bf16_f32 v80, v197, v208
	v_cvt_pk_bf16_f32 v81, v209, v210
	v_cvt_pk_bf16_f32 v82, v211, v220
	v_cvt_pk_bf16_f32 v83, v221, v222
	v_cvt_pk_bf16_f32 v84, v223, v224
	v_cvt_pk_bf16_f32 v85, v225, v226
	v_cvt_pk_bf16_f32 v86, v227, v228
	v_cvt_pk_bf16_f32 v87, v229, v230
	v_cvt_pk_bf16_f32 v88, v201, v202
	v_cvt_pk_bf16_f32 v89, v203, v204
	v_cvt_pk_bf16_f32 v90, v205, v206
	v_cvt_pk_bf16_f32 v91, v207, v231
	v_cvt_pk_bf16_f32 v92, v232, v233
	v_cvt_pk_bf16_f32 v93, v234, v235
	v_cvt_pk_bf16_f32 v94, v236, v237
	v_cvt_pk_bf16_f32 v95, v238, v95
.Lc1_794:
	ds_read_b64_tr_b16 v[202:203], v192 offset:1024
	ds_read_b64_tr_b16 v[204:205], v192 offset:3072
	ds_read_b64_tr_b16 v[206:207], v192 offset:5120
	ds_read_b64_tr_b16 v[208:209], v192 offset:7168
	ds_read_b64_tr_b16 v[222:223], v192 offset:9216
	ds_read_b64_tr_b16 v[224:225], v192 offset:11264
	ds_read_b64_tr_b16 v[226:227], v192 offset:13312
	ds_read_b64_tr_b16 v[228:229], v192 offset:15360
	s_waitcnt lgkmcnt(0)
	v_mfma_f32_32x32x16_bf16 v[0:15], v[80:83], v[202:205], v[0:15]
	ds_read_b64_tr_b16 v[202:203], v192 offset:1536
	ds_read_b64_tr_b16 v[204:205], v192 offset:3584
	ds_read_b64_tr_b16 v[138:139], v192 offset:9728
	ds_read_b64_tr_b16 v[140:141], v192 offset:11776
	v_mfma_f32_32x32x16_bf16 v[0:15], v[84:87], v[206:209], v[0:15]
	ds_read_b64_tr_b16 v[206:207], v192 offset:5632
	ds_read_b64_tr_b16 v[208:209], v192 offset:7680
	ds_read_b64_tr_b16 v[142:143], v192 offset:13824
	ds_read_b64_tr_b16 v[144:145], v192 offset:15872
	v_mfma_f32_32x32x16_bf16 v[0:15], v[88:91], v[222:225], v[0:15]
	s_add_i32 m0, s84, 0x8400
	s_add_u32 s66, s78, s65
	s_addc_u32 s67, s79, 0
	global_load_lds_dwordx4 v185, s[66:67]
	v_mfma_f32_32x32x16_bf16 v[0:15], v[92:95], v[226:229], v[0:15]
	s_waitcnt lgkmcnt(0)
	v_mfma_f32_32x32x16_bf16 v[48:63], v[80:83], v[202:205], v[48:63]
	ds_read_b64_tr_b16 v[202:203], v192 offset:2048
	ds_read_b64_tr_b16 v[204:205], v192 offset:4096
	ds_read_b64_tr_b16 v[222:223], v192 offset:10240
	ds_read_b64_tr_b16 v[224:225], v192 offset:12288
	v_mfma_f32_32x32x16_bf16 v[48:63], v[84:87], v[206:209], v[48:63]
	ds_read_b64_tr_b16 v[206:207], v192 offset:6144
	ds_read_b64_tr_b16 v[208:209], v192 offset:8192
	ds_read_b64_tr_b16 v[226:227], v192 offset:14336
	ds_read_b64_tr_b16 v[228:229], v192 offset:16384
	v_mfma_f32_32x32x16_bf16 v[48:63], v[88:91], v[138:141], v[48:63]
	s_add_i32 m0, s84, 0xa400
	s_add_i32 s64, s65, 0x60000
	global_load_lds_dwordx4 v184, s[66:67]
	v_mfma_f32_32x32x16_bf16 v[48:63], v[92:95], v[142:145], v[48:63]
	s_waitcnt lgkmcnt(0)
	v_mfma_f32_32x32x16_bf16 v[32:47], v[80:83], v[202:205], v[32:47]
	ds_read_b64_tr_b16 v[202:203], v192 offset:2560
	ds_read_b64_tr_b16 v[204:205], v192 offset:4608
	ds_read_b64_tr_b16 v[138:139], v192 offset:10752
	ds_read_b64_tr_b16 v[140:141], v192 offset:12800
	v_mfma_f32_32x32x16_bf16 v[32:47], v[84:87], v[206:209], v[32:47]
	ds_read_b64_tr_b16 v[206:207], v192 offset:6656
	ds_read_b64_tr_b16 v[208:209], v192 offset:8704
	ds_read_b64_tr_b16 v[142:143], v192 offset:14848
	ds_read_b64_tr_b16 v[144:145], v192 offset:16896
	v_mfma_f32_32x32x16_bf16 v[32:47], v[88:91], v[222:225], v[32:47]
	s_cmp_eq_u32 s55, 29
	s_cselect_b32 s64, s89, s64
	s_add_i32 m0, s84, 0xc400
	s_add_u32 s70, s80, s64
	s_addc_u32 s71, s81, 0
	global_load_lds_dwordx4 v183, s[70:71]
	v_mfma_f32_32x32x16_bf16 v[32:47], v[92:95], v[226:229], v[32:47]
	s_waitcnt lgkmcnt(0)
	v_mfma_f32_32x32x16_bf16 v[16:31], v[80:83], v[202:205], v[16:31]
	v_max_f32_e32 v80, v96, v97
	v_max3_f32 v81, v64, v65, v66
	v_max3_f32 v80, v80, v98, v99
	v_max3_f32 v81, v81, v67, v68
	v_max3_f32 v80, v80, v100, v101
	v_mfma_f32_32x32x16_bf16 v[16:31], v[84:87], v[206:209], v[16:31]
	v_max3_f32 v81, v81, v69, v70
	v_max3_f32 v80, v80, v102, v103
	v_max3_f32 v81, v81, v71, v72
	v_max3_f32 v80, v80, v104, v105
	v_max3_f32 v81, v81, v73, v74
	v_max3_f32 v80, v80, v106, v107
	v_max3_f32 v81, v81, v75, v76
	v_mfma_f32_32x32x16_bf16 v[16:31], v[88:91], v[138:141], v[16:31]
	s_add_i32 m0, s84, 0xe400
	s_mov_b32 s65, s64
	global_load_lds_dwordx4 v182, s[70:71]
	v_max3_f32 v80, v80, v108, v109
	v_max3_f32 v81, v81, v77, v78
	v_max3_f32 v80, v80, v110, v111
	v_max3_f32 v80, v80, v81, v79
	v_mov_b32_e32 v197, 1.0
	v_mfma_f32_32x32x16_bf16 v[16:31], v[92:95], v[142:145], v[16:31]
	v_cmp_ge_f32_e64 s[0:1], s56, v80
	s_cmp_eq_u64 s[0:1], exec
	s_cbranch_scc1 .Lc1_799
	s_branch .Lc1_802

.Lc1_799:
	v_exp_f32_e32 v159, v96
	v_exp_f32_e32 v161, v97
	v_exp_f32_e32 v157, v98
	v_exp_f32_e32 v160, v99
	v_exp_f32_e32 v155, v100
	v_exp_f32_e32 v158, v101
	v_exp_f32_e32 v154, v102
	v_exp_f32_e32 v156, v103
	v_exp_f32_e32 v151, v104
	v_exp_f32_e32 v153, v105
	v_exp_f32_e32 v149, v106
	v_exp_f32_e32 v152, v107
	v_exp_f32_e32 v147, v108
	v_exp_f32_e32 v150, v109
	v_exp_f32_e32 v146, v110
	v_exp_f32_e32 v148, v111
	v_fma_f32 v80, v193, v179, v195
	v_fma_f32 v179, v80, v198, v199
	s_cmp_gt_u32 s55, 32
	s_waitcnt vmcnt(4) lgkmcnt(0)
	s_barrier
	s_cbranch_scc1 .LBB0_803
	s_add_i32 s55, s55, 2
	v_mov_b32_e32 v193, v197
	ds_read_b128 v[80:83], v134 offset:50176
	ds_read_b128 v[84:87], v134 offset:58368
	ds_read_b128 v[196:199], v135 offset:50176
	ds_read_b128 v[200:203], v135 offset:58368
	s_waitcnt lgkmcnt(2)
	v_mfma_f32_32x32x16_bf16 v[96:111], v[80:83], v[122:125], 0
	v_exp_f32_e32 v204, v72
	v_exp_f32_e32 v205, v73
	v_exp_f32_e32 v206, v74
	v_exp_f32_e32 v207, v75
	v_exp_f32_e32 v208, v76
	v_exp_f32_e32 v209, v77
	v_mfma_f32_32x32x16_bf16 v[80:95], v[84:87], v[122:125], 0
	v_exp_f32_e32 v210, v78
	v_exp_f32_e32 v79, v79
	s_waitcnt lgkmcnt(0)
	v_mfma_f32_32x32x16_bf16 v[96:111], v[196:199], v[126:129], v[96:111]
	v_mfma_f32_32x32x16_bf16 v[80:95], v[200:203], v[126:129], v[80:95]
	ds_read_b128 v[196:199], v136 offset:50176
	ds_read_b128 v[200:203], v136 offset:58368
	s_waitcnt lgkmcnt(0)
	v_mfma_f32_32x32x16_bf16 v[96:111], v[196:199], v[118:121], v[96:111]
	v_mfma_f32_32x32x16_bf16 v[80:95], v[200:203], v[118:121], v[80:95]
	ds_read_b128 v[196:199], v137 offset:50176
	ds_read_b128 v[200:203], v137 offset:58368
	v_exp_f32_e32 v180, v64
	v_add_f32_e32 v64, v161, v159
	v_add_f32_e32 v195, v157, v160
	v_add_f32_e32 v64, v155, v64
	v_add_f32_e32 v195, v158, v195
	v_add_f32_e32 v64, v154, v64
	v_add_f32_e32 v195, v156, v195
	v_add_f32_e32 v64, v151, v64
	v_add_f32_e32 v195, v153, v195
	v_add_f32_e32 v64, v149, v64
	v_add_f32_e32 v195, v152, v195
	v_add_f32_e32 v64, v147, v64
	s_waitcnt lgkmcnt(0)
	v_mfma_f32_32x32x16_bf16 v[96:111], v[196:199], v[114:117], v[96:111]
	v_exp_f32_e32 v197, v65
	v_add_f32_e32 v195, v150, v195
	v_exp_f32_e32 v198, v66
	v_add_f32_e32 v64, v146, v64
	v_exp_f32_e32 v199, v67
	v_add_f32_e32 v195, v148, v195
	v_add_f32_e32 v64, v180, v64
	v_mfma_f32_32x32x16_bf16 v[80:95], v[200:203], v[114:117], v[80:95]
	v_exp_f32_e32 v200, v68
	v_exp_f32_e32 v201, v69
	v_add_f32_e32 v195, v197, v195
	v_exp_f32_e32 v202, v70
	v_add_f32_e32 v64, v198, v64
	v_exp_f32_e32 v203, v71
	v_add_f32_e32 v195, v199, v195
	v_add_f32_e32 v64, v200, v64
	v_add_f32_e32 v195, v201, v195
	v_add_f32_e32 v64, v202, v64
	v_add_f32_e32 v195, v203, v195
	v_add_f32_e32 v64, v204, v64
	v_add_f32_e32 v195, v205, v195
	v_add_f32_e32 v64, v206, v64
	v_add_f32_e32 v195, v207, v195
	v_add_f32_e32 v64, v208, v64
	v_add_f32_e32 v195, v209, v195
	v_add_f32_e32 v64, v210, v64
	v_add_f32_e32 v195, v79, v195
	v_add_f32_e32 v195, v195, v64
	v_cvt_pk_bf16_f32 v64, v159, v161
	v_cvt_pk_bf16_f32 v65, v157, v160
	v_cvt_pk_bf16_f32 v66, v155, v158
	v_cvt_pk_bf16_f32 v67, v154, v156
	v_cvt_pk_bf16_f32 v68, v151, v153
	v_cvt_pk_bf16_f32 v69, v149, v152
	v_cvt_pk_bf16_f32 v70, v147, v150
	v_cvt_pk_bf16_f32 v71, v146, v148
	v_cvt_pk_bf16_f32 v72, v180, v197
	v_cvt_pk_bf16_f32 v73, v198, v199
	v_cvt_pk_bf16_f32 v74, v200, v201
	v_cvt_pk_bf16_f32 v75, v202, v203
	v_cvt_pk_bf16_f32 v76, v204, v205
	v_cvt_pk_bf16_f32 v77, v206, v207
	v_cvt_pk_bf16_f32 v78, v208, v209
	v_cvt_pk_bf16_f32 v79, v210, v79
	ds_read_b64_tr_b16 v[198:199], v192 offset:17408
	ds_read_b64_tr_b16 v[200:201], v192 offset:19456
	ds_read_b64_tr_b16 v[202:203], v192 offset:21504
	ds_read_b64_tr_b16 v[204:205], v192 offset:23552
	ds_read_b64_tr_b16 v[206:207], v192 offset:25600
	ds_read_b64_tr_b16 v[208:209], v192 offset:27648
	ds_read_b64_tr_b16 v[222:223], v192 offset:29696
	ds_read_b64_tr_b16 v[224:225], v192 offset:31744
	s_waitcnt lgkmcnt(0)
	v_mfma_f32_32x32x16_bf16 v[0:15], v[64:67], v[198:201], v[0:15]
	ds_read_b64_tr_b16 v[198:199], v192 offset:17920
	ds_read_b64_tr_b16 v[200:201], v192 offset:19968
	ds_read_b64_tr_b16 v[138:139], v192 offset:26112
	ds_read_b64_tr_b16 v[140:141], v192 offset:28160
	v_mfma_f32_32x32x16_bf16 v[0:15], v[68:71], v[202:205], v[0:15]
	ds_read_b64_tr_b16 v[202:203], v192 offset:22016
	ds_read_b64_tr_b16 v[204:205], v192 offset:24064
	ds_read_b64_tr_b16 v[142:143], v192 offset:30208
	ds_read_b64_tr_b16 v[144:145], v192 offset:32256
	v_mfma_f32_32x32x16_bf16 v[0:15], v[72:75], v[206:209], v[0:15]
	s_add_i32 m0, s84, 0x400
	s_add_u32 s66, s78, s65
	s_addc_u32 s67, s79, 0
	global_load_lds_dwordx4 v185, s[66:67]
	v_mfma_f32_32x32x16_bf16 v[0:15], v[76:79], v[222:225], v[0:15]
	s_waitcnt lgkmcnt(0)
	v_mfma_f32_32x32x16_bf16 v[48:63], v[64:67], v[198:201], v[48:63]
	ds_read_b64_tr_b16 v[198:199], v192 offset:18432
	ds_read_b64_tr_b16 v[200:201], v192 offset:20480
	ds_read_b64_tr_b16 v[206:207], v192 offset:26624
	ds_read_b64_tr_b16 v[208:209], v192 offset:28672
	v_mfma_f32_32x32x16_bf16 v[48:63], v[68:71], v[202:205], v[48:63]
	ds_read_b64_tr_b16 v[202:203], v192 offset:22528
	ds_read_b64_tr_b16 v[204:205], v192 offset:24576
	ds_read_b64_tr_b16 v[222:223], v192 offset:30720
	ds_read_b64_tr_b16 v[224:225], v192 offset:32768
	v_mfma_f32_32x32x16_bf16 v[48:63], v[72:75], v[138:141], v[48:63]
	s_add_i32 m0, s84, 0x2400
	s_add_i32 s64, s65, 0x60000
	global_load_lds_dwordx4 v184, s[66:67]
	v_mfma_f32_32x32x16_bf16 v[48:63], v[76:79], v[142:145], v[48:63]
	s_waitcnt lgkmcnt(0)
	v_mfma_f32_32x32x16_bf16 v[32:47], v[64:67], v[198:201], v[32:47]
	ds_read_b64_tr_b16 v[198:199], v192 offset:18944
	ds_read_b64_tr_b16 v[200:201], v192 offset:20992
	ds_read_b64_tr_b16 v[138:139], v192 offset:27136
	ds_read_b64_tr_b16 v[140:141], v192 offset:29184
	v_mfma_f32_32x32x16_bf16 v[32:47], v[68:71], v[202:205], v[32:47]
	ds_read_b64_tr_b16 v[202:203], v192 offset:23040
	ds_read_b64_tr_b16 v[204:205], v192 offset:25088
	ds_read_b64_tr_b16 v[142:143], v192 offset:31232
	ds_read_b64_tr_b16 v[144:145], v192 offset:33280
	v_mfma_f32_32x32x16_bf16 v[32:47], v[72:75], v[206:209], v[32:47]
	s_add_i32 m0, s84, 0x10400
	s_add_u32 s70, s80, s64
	s_addc_u32 s71, s81, 0
	global_load_lds_dwordx4 v183, s[70:71]
	v_mfma_f32_32x32x16_bf16 v[32:47], v[76:79], v[222:225], v[32:47]
	s_waitcnt lgkmcnt(0)
	v_mfma_f32_32x32x16_bf16 v[16:31], v[64:67], v[198:201], v[16:31]
	v_max_f32_e32 v64, v96, v97
	v_max3_f32 v65, v80, v81, v82
	v_max3_f32 v64, v64, v98, v99
	v_max3_f32 v65, v65, v83, v84
	v_max3_f32 v64, v64, v100, v101
	v_mfma_f32_32x32x16_bf16 v[16:31], v[68:71], v[202:205], v[16:31]
	v_max3_f32 v65, v65, v85, v86
	v_max3_f32 v64, v64, v102, v103
	v_max3_f32 v65, v65, v87, v88
	v_max3_f32 v64, v64, v104, v105
	v_max3_f32 v65, v65, v89, v90
	v_max3_f32 v64, v64, v106, v107
	v_max3_f32 v65, v65, v91, v92
	v_mfma_f32_32x32x16_bf16 v[16:31], v[72:75], v[138:141], v[16:31]
	s_add_i32 m0, s84, 0x12400
	s_mov_b32 s65, s64
	global_load_lds_dwordx4 v182, s[70:71]
	v_max3_f32 v64, v64, v108, v109
	v_max3_f32 v65, v65, v93, v94
	v_max3_f32 v64, v64, v110, v111
	v_max3_f32 v64, v64, v65, v95
	v_mov_b32_e32 v198, 1.0
	v_mfma_f32_32x32x16_bf16 v[16:31], v[76:79], v[142:145], v[16:31]
	v_cmp_ge_f32_e64 s[0:1], s56, v64
	s_cmp_eq_u64 s[0:1], exec
	s_cbranch_scc1 .Lc2_792
	s_branch .Lc2_801

.Lc2_792:
	v_exp_f32_e32 v197, v96
	v_exp_f32_e32 v208, v97
	v_exp_f32_e32 v209, v98
	v_exp_f32_e32 v210, v99
	v_exp_f32_e32 v211, v100
	v_exp_f32_e32 v220, v101
	v_exp_f32_e32 v221, v102
	v_exp_f32_e32 v222, v103
	v_exp_f32_e32 v223, v104
	v_exp_f32_e32 v224, v105
	v_exp_f32_e32 v225, v106
	v_exp_f32_e32 v226, v107
	v_exp_f32_e32 v227, v108
	v_exp_f32_e32 v228, v109
	v_exp_f32_e32 v229, v110
	v_exp_f32_e32 v230, v111
	s_waitcnt vmcnt(4) lgkmcnt(0)
	s_barrier
	ds_read_b128 v[64:67], v130 offset:50176
	ds_read_b128 v[68:71], v130 offset:58368
	ds_read_b128 v[200:203], v131 offset:50176
	ds_read_b128 v[204:207], v131 offset:58368
	v_exp_f32_e32 v231, v87
	s_waitcnt lgkmcnt(2)
	v_mfma_f32_32x32x16_bf16 v[96:111], v[64:67], v[122:125], 0
	v_exp_f32_e32 v232, v88
	v_exp_f32_e32 v233, v89
	v_exp_f32_e32 v234, v90
	v_exp_f32_e32 v235, v91
	v_exp_f32_e32 v236, v92
	v_exp_f32_e32 v237, v93
	v_exp_f32_e32 v238, v94
	v_mfma_f32_32x32x16_bf16 v[64:79], v[68:71], v[122:125], 0
	v_exp_f32_e32 v95, v95
	s_waitcnt lgkmcnt(0)
	v_mfma_f32_32x32x16_bf16 v[96:111], v[200:203], v[126:129], v[96:111]
	v_mfma_f32_32x32x16_bf16 v[64:79], v[204:207], v[126:129], v[64:79]
	ds_read_b128 v[200:203], v132 offset:50176
	ds_read_b128 v[204:207], v132 offset:58368
	s_waitcnt lgkmcnt(0)
	v_mfma_f32_32x32x16_bf16 v[96:111], v[200:203], v[118:121], v[96:111]
	v_mfma_f32_32x32x16_bf16 v[64:79], v[204:207], v[118:121], v[64:79]
	ds_read_b128 v[200:203], v133 offset:50176
	ds_read_b128 v[204:207], v133 offset:58368
	s_waitcnt lgkmcnt(0)
	v_mfma_f32_32x32x16_bf16 v[96:111], v[200:203], v[114:117], v[96:111]
	v_exp_f32_e32 v201, v80
	v_add_f32_e32 v80, v208, v197
	v_add_f32_e32 v199, v209, v210
	v_add_f32_e32 v80, v211, v80
	v_add_f32_e32 v199, v220, v199
	v_add_f32_e32 v80, v221, v80
	v_add_f32_e32 v199, v222, v199
	v_add_f32_e32 v80, v223, v80
	v_add_f32_e32 v199, v224, v199
	v_add_f32_e32 v80, v225, v80
	v_add_f32_e32 v199, v226, v199
	v_add_f32_e32 v80, v227, v80
	v_exp_f32_e32 v202, v81
	v_add_f32_e32 v199, v228, v199
	v_exp_f32_e32 v203, v82
	v_add_f32_e32 v80, v229, v80
	v_mfma_f32_32x32x16_bf16 v[64:79], v[204:207], v[114:117], v[64:79]
	v_exp_f32_e32 v204, v83
	v_add_f32_e32 v199, v230, v199
	v_exp_f32_e32 v205, v84
	v_add_f32_e32 v80, v201, v80
	v_exp_f32_e32 v206, v85
	v_add_f32_e32 v199, v202, v199
	v_exp_f32_e32 v207, v86
	v_add_f32_e32 v80, v203, v80
	v_add_f32_e32 v199, v204, v199
	v_add_f32_e32 v80, v205, v80
	v_add_f32_e32 v199, v206, v199
	v_add_f32_e32 v80, v207, v80
	v_add_f32_e32 v199, v231, v199
	v_add_f32_e32 v80, v232, v80
	v_add_f32_e32 v199, v233, v199
	v_add_f32_e32 v80, v234, v80
	v_add_f32_e32 v199, v235, v199
	v_add_f32_e32 v80, v236, v80
	v_add_f32_e32 v199, v237, v199
	v_add_f32_e32 v80, v238, v80
	v_add_f32_e32 v199, v95, v199
	v_add_f32_e32 v199, v199, v80
	v_cvt_pk_bf16_f32 v80, v197, v208
	v_cvt_pk_bf16_f32 v81, v209, v210
	v_cvt_pk_bf16_f32 v82, v211, v220
	v_cvt_pk_bf16_f32 v83, v221, v222
	v_cvt_pk_bf16_f32 v84, v223, v224
	v_cvt_pk_bf16_f32 v85, v225, v226
	v_cvt_pk_bf16_f32 v86, v227, v228
	v_cvt_pk_bf16_f32 v87, v229, v230
	v_cvt_pk_bf16_f32 v88, v201, v202
	v_cvt_pk_bf16_f32 v89, v203, v204
	v_cvt_pk_bf16_f32 v90, v205, v206
	v_cvt_pk_bf16_f32 v91, v207, v231
	v_cvt_pk_bf16_f32 v92, v232, v233
	v_cvt_pk_bf16_f32 v93, v234, v235
	v_cvt_pk_bf16_f32 v94, v236, v237
	v_cvt_pk_bf16_f32 v95, v238, v95
.Lc2_794:
	ds_read_b64_tr_b16 v[202:203], v192 offset:33792
	ds_read_b64_tr_b16 v[204:205], v192 offset:35840
	ds_read_b64_tr_b16 v[206:207], v192 offset:37888
	ds_read_b64_tr_b16 v[208:209], v192 offset:39936
	ds_read_b64_tr_b16 v[222:223], v192 offset:41984
	ds_read_b64_tr_b16 v[224:225], v192 offset:44032
	ds_read_b64_tr_b16 v[226:227], v192 offset:46080
	ds_read_b64_tr_b16 v[228:229], v192 offset:48128
	s_waitcnt lgkmcnt(0)
	v_mfma_f32_32x32x16_bf16 v[0:15], v[80:83], v[202:205], v[0:15]
	ds_read_b64_tr_b16 v[202:203], v192 offset:34304
	ds_read_b64_tr_b16 v[204:205], v192 offset:36352
	ds_read_b64_tr_b16 v[138:139], v192 offset:42496
	ds_read_b64_tr_b16 v[140:141], v192 offset:44544
	v_mfma_f32_32x32x16_bf16 v[0:15], v[84:87], v[206:209], v[0:15]
	ds_read_b64_tr_b16 v[206:207], v192 offset:38400
	ds_read_b64_tr_b16 v[208:209], v192 offset:40448
	ds_read_b64_tr_b16 v[142:143], v192 offset:46592
	ds_read_b64_tr_b16 v[144:145], v192 offset:48640
	v_mfma_f32_32x32x16_bf16 v[0:15], v[88:91], v[222:225], v[0:15]
	s_add_i32 m0, s84, 0x4400
	s_add_u32 s66, s78, s65
	s_addc_u32 s67, s79, 0
	global_load_lds_dwordx4 v185, s[66:67]
	v_mfma_f32_32x32x16_bf16 v[0:15], v[92:95], v[226:229], v[0:15]
	s_waitcnt lgkmcnt(0)
	v_mfma_f32_32x32x16_bf16 v[48:63], v[80:83], v[202:205], v[48:63]
	ds_read_b64_tr_b16 v[202:203], v192 offset:34816
	ds_read_b64_tr_b16 v[204:205], v192 offset:36864
	ds_read_b64_tr_b16 v[222:223], v192 offset:43008
	ds_read_b64_tr_b16 v[224:225], v192 offset:45056
	v_mfma_f32_32x32x16_bf16 v[48:63], v[84:87], v[206:209], v[48:63]
	ds_read_b64_tr_b16 v[206:207], v192 offset:38912
	ds_read_b64_tr_b16 v[208:209], v192 offset:40960
	ds_read_b64_tr_b16 v[226:227], v192 offset:47104
	ds_read_b64_tr_b16 v[228:229], v192 offset:49152
	v_mfma_f32_32x32x16_bf16 v[48:63], v[88:91], v[138:141], v[48:63]
	s_add_i32 m0, s84, 0x6400
	s_add_i32 s64, s65, 0x60000
	global_load_lds_dwordx4 v184, s[66:67]
	v_mfma_f32_32x32x16_bf16 v[48:63], v[92:95], v[142:145], v[48:63]
	s_waitcnt lgkmcnt(0)
	v_mfma_f32_32x32x16_bf16 v[32:47], v[80:83], v[202:205], v[32:47]
	ds_read_b64_tr_b16 v[202:203], v192 offset:35328
	ds_read_b64_tr_b16 v[204:205], v192 offset:37376
	ds_read_b64_tr_b16 v[138:139], v192 offset:43520
	ds_read_b64_tr_b16 v[140:141], v192 offset:45568
	v_mfma_f32_32x32x16_bf16 v[32:47], v[84:87], v[206:209], v[32:47]
	ds_read_b64_tr_b16 v[206:207], v192 offset:39424
	ds_read_b64_tr_b16 v[208:209], v192 offset:41472
	ds_read_b64_tr_b16 v[142:143], v192 offset:47616
	ds_read_b64_tr_b16 v[144:145], v192 offset:49664
	v_mfma_f32_32x32x16_bf16 v[32:47], v[88:91], v[222:225], v[32:47]
	s_cmp_eq_u32 s55, 29
	s_cselect_b32 s64, s89, s64
	s_add_i32 m0, s84, 0x14400
	s_add_u32 s70, s80, s64
	s_addc_u32 s71, s81, 0
	global_load_lds_dwordx4 v183, s[70:71]
	v_mfma_f32_32x32x16_bf16 v[32:47], v[92:95], v[226:229], v[32:47]
	s_waitcnt lgkmcnt(0)
	v_mfma_f32_32x32x16_bf16 v[16:31], v[80:83], v[202:205], v[16:31]
	v_max_f32_e32 v80, v96, v97
	v_max3_f32 v81, v64, v65, v66
	v_max3_f32 v80, v80, v98, v99
	v_max3_f32 v81, v81, v67, v68
	v_max3_f32 v80, v80, v100, v101
	v_mfma_f32_32x32x16_bf16 v[16:31], v[84:87], v[206:209], v[16:31]
	v_max3_f32 v81, v81, v69, v70
	v_max3_f32 v80, v80, v102, v103
	v_max3_f32 v81, v81, v71, v72
	v_max3_f32 v80, v80, v104, v105
	v_max3_f32 v81, v81, v73, v74
	v_max3_f32 v80, v80, v106, v107
	v_max3_f32 v81, v81, v75, v76
	v_mfma_f32_32x32x16_bf16 v[16:31], v[88:91], v[138:141], v[16:31]
	s_add_i32 m0, s84, 0x16400
	s_mov_b32 s65, s64
	global_load_lds_dwordx4 v182, s[70:71]
	v_max3_f32 v80, v80, v108, v109
	v_max3_f32 v81, v81, v77, v78
	v_max3_f32 v80, v80, v110, v111
	v_max3_f32 v80, v80, v81, v79
	v_mov_b32_e32 v197, 1.0
	v_mfma_f32_32x32x16_bf16 v[16:31], v[92:95], v[142:145], v[16:31]
	v_cmp_ge_f32_e64 s[0:1], s56, v80
	s_cmp_eq_u64 s[0:1], exec
	s_cbranch_scc1 .Lc2_799
	s_branch .Lc2_802
